# v10 with late L2 warm-up issued before the phase-A barrier
# speedup vs baseline: 1.0393x; 1.0393x over previous
.LBB2_414:
	s_movk_i32 s0, 0xc00
	v_mov_b64_e32 v[26:27], s[42:43]
	v_mul_u32_u24_e32 v28, 0xc00, v154
	v_mad_i64_i32 v[26:27], s[0:1], v62, s0, v[26:27]
	v_or_b32_e32 v28, v28, v98
	v_mov_b32_e32 v99, 0
	v_lshl_add_u64 v[26:27], v[26:27], 0, v[98:99]
	v_or_b32_e32 v29, 0x10000, v28
	global_store_dwordx4 v[26:27], v[22:25], off sc1
	ds_write_b128 v29, v[22:25]
	v_sub_f32_e32 v10, v10, v22
	v_or_b32_e32 v22, v101, v154
	v_sub_f32_e32 v11, v11, v23
	v_add_u32_e32 v23, v22, v102
	v_lshl_or_b32 v23, v23, 4, v103
	ds_write_b32 v23, v10
	v_add_u32_e32 v10, v22, v104
	v_lshl_or_b32 v10, v10, 4, v105
	ds_write_b32 v10, v11
	v_or_b32_e32 v10, v106, v154
	v_add_u32_e32 v10, v10, v107
	v_sub_f32_e32 v12, v12, v24
	v_lshl_or_b32 v10, v10, 4, v108
	ds_write_b32 v10, v12
	v_or_b32_e32 v10, v109, v154
	v_add_u32_e32 v10, v10, v110
	v_sub_f32_e32 v13, v13, v25
	v_lshl_or_b32 v10, v10, 4, v111
	ds_write_b32 v10, v13
	v_add_u32_e32 v10, 0x10400, v28
	ds_write_b128 v10, v[18:21]
	v_sub_f32_e32 v10, v6, v18
	v_sub_f32_e32 v11, v7, v19
	v_pk_add_f32 v[6:7], v[8:9], v[20:21] neg_lo:[0,1] neg_hi:[0,1]
	v_or_b32_e32 v8, v112, v154
	v_add_u32_e32 v9, v8, v113
	v_add_u32_e32 v8, v8, v115
	v_lshl_or_b32 v9, v9, 4, v114
	v_lshl_or_b32 v8, v8, 4, v116
	ds_write_b32 v9, v10
	ds_write_b32 v8, v11
	v_or_b32_e32 v8, v117, v154
	v_add_u32_e32 v8, v8, v118
	v_lshl_or_b32 v8, v8, 4, v119
	ds_write_b32 v8, v6
	v_or_b32_e32 v6, v120, v154
	v_add_u32_e32 v6, v6, v121
	v_lshl_or_b32 v6, v6, 4, v122
	ds_write_b32 v6, v7
	v_add_u32_e32 v6, 0x10800, v28
	ds_write_b128 v6, v[14:17]
	v_or_b32_e32 v6, v123, v154
	v_add_u32_e32 v7, v6, v124
	v_pk_add_f32 v[2:3], v[2:3], v[14:15] neg_lo:[0,1] neg_hi:[0,1]
	v_lshl_or_b32 v7, v7, 4, v125
	ds_write_b32 v7, v2
	v_add_u32_e32 v2, v6, v126
	v_lshl_or_b32 v2, v2, 4, v127
	ds_write_b32 v2, v3
	v_or_b32_e32 v2, v133, v154
	v_add_u32_e32 v2, v2, v134
	v_pk_add_f32 v[4:5], v[4:5], v[16:17] neg_lo:[0,1] neg_hi:[0,1]
	v_lshl_or_b32 v2, v2, 4, v63
	ds_write_b32 v2, v4
	v_or_b32_e32 v2, v135, v154
	v_add_u32_e32 v2, v2, v132
	v_lshl_or_b32 v2, v2, 4, v136
	v_add_lshl_u32 v4, v100, v154, 4
	s_mov_b32 s5, 0
	s_mov_b32 s4, 1.0
	ds_write_b32 v2, v5
	v_mov_b64_e32 v[2:3], s[4:5]
	v_add_u32_e32 v4, 8, v4
	s_waitcnt vmcnt(1)
	v_lshlrev_b32_e32 v40, 9, v150
	ds_write2st64_b64 v4, v[2:3], v[2:3] offset1:64
	v_or_b32_e32 v2, v40, v128
	v_lshlrev_b32_e32 v98, 4, v2
	v_lshl_add_u64 v[100:101], s[40:41], 0, v[98:99]
	s_mov_b64 s[0:1], 0x787000
	v_lshl_add_u64 v[34:35], v[100:101], 0, s[0:1]
	s_mov_b32 s0, 0x788000
	v_add_co_u32_e32 v36, vcc, s0, v100
	global_store_dwordx4 v[26:27], v[18:21], off offset:1024 sc1
	global_store_dwordx4 v[26:27], v[14:17], off offset:2048 sc1
	s_lshr_b32 s59, s33, 4
	s_and_b32 s59, s59, 31
	s_lshl_b32 s59, s59, 15
	s_add_u32 s59, s59, 0x787000
	s_add_u32 s68, s40, s59
	s_addc_u32 s69, s41, 0
	v_lshlrev_b32_e32 v207, 6, v0
	global_load_dword v207, v207, s[68:69]
	s_waitcnt lgkmcnt(0)
	s_barrier
	v_addc_co_u32_e32 v37, vcc, 0, v101, vcc
	global_load_dwordx4 v[2:5], v[34:35], off offset:1024
	global_load_dwordx4 v[10:13], v[34:35], off offset:2048
	global_load_dwordx4 v[14:17], v[34:35], off offset:3072
	global_load_dwordx4 v[6:9], v[36:37], off offset:-4096
	global_load_dwordx4 v[18:21], v[36:37], off
	global_load_dwordx4 v[22:25], v[36:37], off offset:1024
	global_load_dwordx4 v[26:29], v[36:37], off offset:2048
	global_load_dwordx4 v[30:33], v[36:37], off offset:3072
	v_and_b32_e32 v35, 15, v0
	v_lshrrev_b32_e32 v37, 4, v128
	v_lshlrev_b32_e32 v102, 2, v35
	v_lshlrev_b32_e32 v41, 2, v37
	v_lshlrev_b32_e32 v34, 4, v35
	v_cmp_gt_u32_e64 s[0:1], 6, v35
	v_mov_b32_e32 v35, v99
	v_or3_b32 v36, v34, v41, v40
	v_lshl_add_u64 v[104:105], s[44:45], 0, v[34:35]
	v_or_b32_e32 v34, v40, v34
	s_movk_i32 s4, 0x1000
	v_or3_b32 v153, v34, v41, s4
	v_or_b32_e32 v34, 0x11800, v98
	v_lshl_add_u64 v[118:119], s[40:41], 0, v[34:35]
	v_or_b32_e32 v34, 0x11400, v98
	v_lshl_add_u64 v[120:121], s[40:41], 0, v[34:35]
	v_or_b32_e32 v34, 0x11000, v98
	ds_read2st64_b32 v[132:133], v36 offset1:1
	v_or_b32_e32 v36, s33, v41
	v_lshl_add_u64 v[122:123], s[40:41], 0, v[34:35]
	v_or_b32_e32 v34, 0x10c00, v98
	v_or_b32_e32 v38, 1, v36
	v_lshl_add_u64 v[124:125], s[40:41], 0, v[34:35]
	v_or_b32_e32 v34, 0x10800, v98
	v_mul_u32_u24_e32 v152, 0x3000, v37
	v_ashrrev_i32_e32 v37, 31, v36
	v_ashrrev_i32_e32 v39, 31, v38
	v_lshl_add_u64 v[126:127], s[40:41], 0, v[34:35]
	v_or_b32_e32 v34, 0x10400, v98
	v_mov_b32_e32 v103, v99
	v_lshlrev_b64 v[108:109], 17, v[36:37]
	v_lshlrev_b64 v[110:111], 17, v[38:39]
	v_or_b32_e32 v38, 2, v36
	v_or_b32_e32 v36, 3, v36
	v_lshl_add_u64 v[128:129], s[40:41], 0, v[34:35]
	v_mul_u32_u24_e32 v34, 24, v150
	v_lshl_add_u64 v[106:107], s[38:39], 0, v[102:103]
	v_ashrrev_i32_e32 v39, 31, v38
	v_ashrrev_i32_e32 v37, 31, v36
	v_lshlrev_b32_e32 v103, 2, v0
	v_or_b32_e32 v98, 0x11c00, v98
	v_or_b32_e32 v34, v152, v34
	v_lshlrev_b64 v[112:113], 17, v[38:39]
	v_lshlrev_b64 v[114:115], 17, v[36:37]
	v_and_b32_e32 v116, 0x700, v103
	v_mov_b32_e32 v117, v99
	v_lshl_add_u64 v[130:131], s[40:41], 0, v[98:99]
	v_add_u32_e32 v154, v34, v102
	s_mov_b64 s[6:7], 0
	s_mov_b64 s[8:9], 0x800
	v_mov_b32_e32 v155, 0x400
	v_mov_b32_e32 v159, 0
	v_mov_b32_e32 v158, 0
	v_mov_b32_e32 v157, 0
	v_mov_b32_e32 v156, 0
	s_waitcnt vmcnt(0)
	s_branch .LBB2_417
